# v5_vgprD
# speedup vs baseline: 1.0279x; 1.0279x over previous
.LBB1_104:
	s_lshl_b32 s96, s59, 4
	v_or_b32_e32 v164, s96, v131
	s_andn2_b64 vcc, exec, s[54:55]
	v_lshlrev_b32_e32 v163, 2, v164
	s_cbranch_vccnz .LBB1_114
	v_or_b32_e32 v66, s96, v130
	v_mul_lo_u32 v165, v66, s95
	v_add3_u32 v68, v163, v165, s85
	v_mov_b32_e32 v72, v68
	s_nop 0
	ds_read2_b32 v[66:67], v72 offset1:68
	ds_read2_b32 v[68:69], v72 offset0:136 offset1:204
	v_accvgpr_write_b32 a4, v137
	v_accvgpr_write_b32 a5, v138
	v_accvgpr_write_b32 a6, v139
	s_waitcnt lgkmcnt(1)
	v_readlane_b32 s54, v66, 0
	v_accvgpr_write_b32 a7, v140
	v_cmp_lt_i32_e32 vcc, 0, v136
	v_rcp_f32_e64 v73, -s54
	v_cndmask_b32_e64 v72, 0, v66, s[6:7]
	v_mul_f32_e32 v70, v72, v73
	s_waitcnt lgkmcnt(0)
	s_nop 0
	v_mfma_f32_16x16x4_f32 v[66:69], v70, v66, v[66:69]
	v_mfma_f32_16x16x4_f32 a[4:7], v70, v137, a[4:7]
	s_nop 5
	v_readlane_b32 s54, v67, 1
	v_cndmask_b32_e64 v72, 0, v67, s[8:9]
	s_nop 0
	v_rcp_f32_e64 v73, -s54
	s_nop 0
	v_mul_f32_e32 v71, v72, v73
	s_nop 1
	v_mfma_f32_16x16x4_f32 v[66:69], v71, v67, v[66:69]
	v_mfma_f32_16x16x4_f32 a[4:7], v71, a5, a[4:7]
	s_nop 5
	v_readlane_b32 s54, v68, 2
	v_cndmask_b32_e64 v72, 0, v68, s[10:11]
	s_nop 0
	v_rcp_f32_e64 v73, -s54
	s_nop 0
	v_mul_f32_e32 v70, v72, v73
	s_nop 1
	v_mfma_f32_16x16x4_f32 v[66:69], v70, v68, v[66:69]
	v_mfma_f32_16x16x4_f32 a[4:7], v70, a6, a[4:7]
	s_nop 5
	v_readlane_b32 s54, v69, 3
	v_cndmask_b32_e64 v72, 0, v69, s[12:13]
	s_nop 0
	v_rcp_f32_e64 v73, -s54
	s_nop 0
	v_mul_f32_e32 v71, v72, v73
	s_nop 1
	v_mfma_f32_16x16x4_f32 v[66:69], v71, v69, v[66:69]
	v_mfma_f32_16x16x4_f32 a[4:7], v71, a7, a[4:7]
	s_nop 5
	v_readlane_b32 s54, v66, 20
	v_cndmask_b32_e64 v72, 0, v66, s[14:15]
	s_nop 0
	v_rcp_f32_e64 v73, -s54
	s_nop 0
	v_mul_f32_e32 v70, v72, v73
	s_nop 1
	v_mfma_f32_16x16x4_f32 v[66:69], v70, v66, v[66:69]
	v_mfma_f32_16x16x4_f32 a[4:7], v70, a4, a[4:7]
	s_nop 5
	v_readlane_b32 s54, v67, 21
	v_cndmask_b32_e64 v72, 0, v67, s[16:17]
	s_nop 0
	v_rcp_f32_e64 v73, -s54
	s_nop 0
	v_mul_f32_e32 v71, v72, v73
	s_nop 1
	v_mfma_f32_16x16x4_f32 v[66:69], v71, v67, v[66:69]
	v_mfma_f32_16x16x4_f32 a[4:7], v71, a5, a[4:7]
	s_nop 5
	v_readlane_b32 s54, v68, 22
	v_cndmask_b32_e64 v72, 0, v68, s[18:19]
	s_nop 0
	v_rcp_f32_e64 v73, -s54
	s_nop 0
	v_mul_f32_e32 v70, v72, v73
	s_nop 1
	v_mfma_f32_16x16x4_f32 v[66:69], v70, v68, v[66:69]
	v_mfma_f32_16x16x4_f32 a[4:7], v70, a6, a[4:7]
	s_nop 5
	v_readlane_b32 s54, v69, 23
	v_cndmask_b32_e64 v72, 0, v69, s[20:21]
	s_nop 0
	v_rcp_f32_e64 v73, -s54
	s_nop 0
	v_mul_f32_e32 v71, v72, v73
	s_nop 1
	v_mfma_f32_16x16x4_f32 v[66:69], v71, v69, v[66:69]
	v_mfma_f32_16x16x4_f32 a[4:7], v71, a7, a[4:7]
	s_nop 5
	v_readlane_b32 s54, v66, 40
	v_cndmask_b32_e64 v72, 0, v66, s[22:23]
	s_nop 0
	v_rcp_f32_e64 v73, -s54
	s_nop 0
	v_mul_f32_e32 v70, v72, v73
	s_nop 1
	v_mfma_f32_16x16x4_f32 v[66:69], v70, v66, v[66:69]
	v_mfma_f32_16x16x4_f32 a[4:7], v70, a4, a[4:7]
	s_nop 5
	v_readlane_b32 s54, v67, 41
	v_cndmask_b32_e64 v72, 0, v67, s[24:25]
	s_nop 0
	v_rcp_f32_e64 v73, -s54
	s_nop 0
	v_mul_f32_e32 v71, v72, v73
	s_nop 1
	v_mfma_f32_16x16x4_f32 v[66:69], v71, v67, v[66:69]
	v_mfma_f32_16x16x4_f32 a[4:7], v71, a5, a[4:7]
	s_nop 5
	v_readlane_b32 s54, v68, 42
	v_cndmask_b32_e64 v72, 0, v68, s[26:27]
	s_nop 0
	v_rcp_f32_e64 v73, -s54
	s_nop 0
	v_mul_f32_e32 v70, v72, v73
	s_nop 1
	v_mfma_f32_16x16x4_f32 v[66:69], v70, v68, v[66:69]
	v_mfma_f32_16x16x4_f32 a[4:7], v70, a6, a[4:7]
	s_nop 5
	v_readlane_b32 s54, v69, 43
	v_cndmask_b32_e64 v72, 0, v69, s[28:29]
	s_nop 0
	v_rcp_f32_e64 v73, -s54
	s_nop 0
	v_mul_f32_e32 v71, v72, v73
	s_nop 1
	v_mfma_f32_16x16x4_f32 v[66:69], v71, v69, v[66:69]
	v_mfma_f32_16x16x4_f32 a[4:7], v71, a7, a[4:7]
	s_nop 5
	v_readlane_b32 s54, v66, 60
	v_cndmask_b32_e64 v72, 0, v66, s[30:31]
	s_nop 0
	v_rcp_f32_e64 v73, -s54
	s_nop 0
	v_mul_f32_e32 v70, v72, v73
	s_nop 1
	v_mfma_f32_16x16x4_f32 v[66:69], v70, v66, v[66:69]
	v_mfma_f32_16x16x4_f32 a[4:7], v70, a4, a[4:7]
	s_nop 5
	v_readlane_b32 s54, v67, 61
	v_cndmask_b32_e64 v72, 0, v67, s[34:35]
	s_nop 0
	v_rcp_f32_e64 v73, -s54
	s_nop 0
	v_mul_f32_e32 v71, v72, v73
	s_nop 1
	v_mfma_f32_16x16x4_f32 v[66:69], v71, v67, v[66:69]
	v_mfma_f32_16x16x4_f32 a[4:7], v71, a5, a[4:7]
	s_nop 5
	v_readlane_b32 s54, v68, 62
	v_cndmask_b32_e64 v72, 0, v68, s[36:37]
	s_nop 0
	v_rcp_f32_e64 v73, -s54
	s_nop 0
	v_mul_f32_e32 v70, v72, v73
	s_nop 1
	v_mfma_f32_16x16x4_f32 v[66:69], v70, v68, v[66:69]
	v_mfma_f32_16x16x4_f32 a[4:7], v70, a6, a[4:7]
	s_nop 5
	ds_bpermute_b32 v166, v135, v66
	ds_bpermute_b32 v167, v135, v67
	ds_bpermute_b32 v168, v135, v68
	ds_bpermute_b32 v169, v135, v69
	v_accvgpr_read_b32 v73, a7
	v_accvgpr_read_b32 v72, a6
	v_accvgpr_read_b32 v71, a5
	v_accvgpr_read_b32 v70, a4
	s_and_saveexec_b64 s[54:55], vcc
	s_cbranch_execz .LBB1_111
	v_cmp_ne_u32_e32 vcc, 1, v136
	s_and_saveexec_b64 s[56:57], vcc
	s_xor_b64 s[56:57], exec, s[56:57]
	s_cbranch_execz .LBB1_108
	s_waitcnt lgkmcnt(0)
	v_cndmask_b32_e64 v166, v169, v168, s[2:3]

.LBB1_225:
	s_lshl_b32 s97, s59, 4
	v_or_b32_e32 v14, s97, v131
	s_andn2_b64 vcc, exec, s[52:53]
	v_lshlrev_b32_e32 v13, 2, v14
	s_cbranch_vccnz .LBB1_235
	v_or_b32_e32 v2, s97, v130
	v_mul_lo_u32 v15, v2, s57
	v_add3_u32 v4, v13, v15, s95
	v_mov_b32_e32 v8, v4
	s_nop 0
	ds_read2_b32 v[2:3], v8 offset1:68
	ds_read2_b32 v[4:5], v8 offset0:136 offset1:204
	v_accvgpr_write_b32 a4, v137
	v_accvgpr_write_b32 a5, v138
	v_accvgpr_write_b32 a6, v139
	s_waitcnt lgkmcnt(1)
	v_readlane_b32 s52, v2, 0
	v_accvgpr_write_b32 a7, v140
	v_cmp_lt_i32_e32 vcc, 0, v136
	v_rcp_f32_e64 v9, -s52
	v_cndmask_b32_e64 v8, 0, v2, s[6:7]
	v_mul_f32_e32 v6, v8, v9
	s_waitcnt lgkmcnt(0)
	s_nop 0
	v_mfma_f32_16x16x4_f32 v[2:5], v6, v2, v[2:5]
	v_mfma_f32_16x16x4_f32 a[4:7], v6, v137, a[4:7]
	s_nop 5
	v_readlane_b32 s52, v3, 1
	v_cndmask_b32_e64 v8, 0, v3, s[8:9]
	s_nop 0
	v_rcp_f32_e64 v9, -s52
	s_nop 0
	v_mul_f32_e32 v7, v8, v9
	s_nop 1
	v_mfma_f32_16x16x4_f32 v[2:5], v7, v3, v[2:5]
	v_mfma_f32_16x16x4_f32 a[4:7], v7, a5, a[4:7]
	s_nop 5
	v_readlane_b32 s52, v4, 2
	v_cndmask_b32_e64 v8, 0, v4, s[10:11]
	s_nop 0
	v_rcp_f32_e64 v9, -s52
	s_nop 0
	v_mul_f32_e32 v6, v8, v9
	s_nop 1
	v_mfma_f32_16x16x4_f32 v[2:5], v6, v4, v[2:5]
	v_mfma_f32_16x16x4_f32 a[4:7], v6, a6, a[4:7]
	s_nop 5
	v_readlane_b32 s52, v5, 3
	v_cndmask_b32_e64 v8, 0, v5, s[12:13]
	s_nop 0
	v_rcp_f32_e64 v9, -s52
	s_nop 0
	v_mul_f32_e32 v7, v8, v9
	s_nop 1
	v_mfma_f32_16x16x4_f32 v[2:5], v7, v5, v[2:5]
	v_mfma_f32_16x16x4_f32 a[4:7], v7, a7, a[4:7]
	s_nop 5
	v_readlane_b32 s52, v2, 20
	v_cndmask_b32_e64 v8, 0, v2, s[14:15]
	s_nop 0
	v_rcp_f32_e64 v9, -s52
	s_nop 0
	v_mul_f32_e32 v6, v8, v9
	s_nop 1
	v_mfma_f32_16x16x4_f32 v[2:5], v6, v2, v[2:5]
	v_mfma_f32_16x16x4_f32 a[4:7], v6, a4, a[4:7]
	s_nop 5
	v_readlane_b32 s52, v3, 21
	v_cndmask_b32_e64 v8, 0, v3, s[16:17]
	s_nop 0
	v_rcp_f32_e64 v9, -s52
	s_nop 0
	v_mul_f32_e32 v7, v8, v9
	s_nop 1
	v_mfma_f32_16x16x4_f32 v[2:5], v7, v3, v[2:5]
	v_mfma_f32_16x16x4_f32 a[4:7], v7, a5, a[4:7]
	s_nop 5
	v_readlane_b32 s52, v4, 22
	v_cndmask_b32_e64 v8, 0, v4, s[18:19]
	s_nop 0
	v_rcp_f32_e64 v9, -s52
	s_nop 0
	v_mul_f32_e32 v6, v8, v9
	s_nop 1
	v_mfma_f32_16x16x4_f32 v[2:5], v6, v4, v[2:5]
	v_mfma_f32_16x16x4_f32 a[4:7], v6, a6, a[4:7]
	s_nop 5
	v_readlane_b32 s52, v5, 23
	v_cndmask_b32_e64 v8, 0, v5, s[20:21]
	s_nop 0
	v_rcp_f32_e64 v9, -s52
	s_nop 0
	v_mul_f32_e32 v7, v8, v9
	s_nop 1
	v_mfma_f32_16x16x4_f32 v[2:5], v7, v5, v[2:5]
	v_mfma_f32_16x16x4_f32 a[4:7], v7, a7, a[4:7]
	s_nop 5
	v_readlane_b32 s52, v2, 40
	v_cndmask_b32_e64 v8, 0, v2, s[22:23]
	s_nop 0
	v_rcp_f32_e64 v9, -s52
	s_nop 0
	v_mul_f32_e32 v6, v8, v9
	s_nop 1
	v_mfma_f32_16x16x4_f32 v[2:5], v6, v2, v[2:5]
	v_mfma_f32_16x16x4_f32 a[4:7], v6, a4, a[4:7]
	s_nop 5
	v_readlane_b32 s52, v3, 41
	v_cndmask_b32_e64 v8, 0, v3, s[24:25]
	s_nop 0
	v_rcp_f32_e64 v9, -s52
	s_nop 0
	v_mul_f32_e32 v7, v8, v9
	s_nop 1
	v_mfma_f32_16x16x4_f32 v[2:5], v7, v3, v[2:5]
	v_mfma_f32_16x16x4_f32 a[4:7], v7, a5, a[4:7]
	s_nop 5
	v_readlane_b32 s52, v4, 42
	v_cndmask_b32_e64 v8, 0, v4, s[26:27]
	s_nop 0
	v_rcp_f32_e64 v9, -s52
	s_nop 0
	v_mul_f32_e32 v6, v8, v9
	s_nop 1
	v_mfma_f32_16x16x4_f32 v[2:5], v6, v4, v[2:5]
	v_mfma_f32_16x16x4_f32 a[4:7], v6, a6, a[4:7]
	s_nop 5
	v_readlane_b32 s52, v5, 43
	v_cndmask_b32_e64 v8, 0, v5, s[28:29]
	s_nop 0
	v_rcp_f32_e64 v9, -s52
	s_nop 0
	v_mul_f32_e32 v7, v8, v9
	s_nop 1
	v_mfma_f32_16x16x4_f32 v[2:5], v7, v5, v[2:5]
	v_mfma_f32_16x16x4_f32 a[4:7], v7, a7, a[4:7]
	s_nop 5
	v_readlane_b32 s52, v2, 60
	v_cndmask_b32_e64 v8, 0, v2, s[30:31]
	s_nop 0
	v_rcp_f32_e64 v9, -s52
	s_nop 0
	v_mul_f32_e32 v6, v8, v9
	s_nop 1
	v_mfma_f32_16x16x4_f32 v[2:5], v6, v2, v[2:5]
	v_mfma_f32_16x16x4_f32 a[4:7], v6, a4, a[4:7]
	s_nop 5
	v_readlane_b32 s52, v3, 61
	v_cndmask_b32_e64 v8, 0, v3, s[34:35]
	s_nop 0
	v_rcp_f32_e64 v9, -s52
	s_nop 0
	v_mul_f32_e32 v7, v8, v9
	s_nop 1
	v_mfma_f32_16x16x4_f32 v[2:5], v7, v3, v[2:5]
	v_mfma_f32_16x16x4_f32 a[4:7], v7, a5, a[4:7]
	s_nop 5
	v_readlane_b32 s52, v4, 62
	v_cndmask_b32_e64 v8, 0, v4, s[36:37]
	s_nop 0
	v_rcp_f32_e64 v9, -s52
	s_nop 0
	v_mul_f32_e32 v6, v8, v9
	s_nop 1
	v_mfma_f32_16x16x4_f32 v[2:5], v6, v4, v[2:5]
	v_mfma_f32_16x16x4_f32 a[4:7], v6, a6, a[4:7]
	s_nop 5
	ds_bpermute_b32 v16, v135, v2
	ds_bpermute_b32 v17, v135, v3
	ds_bpermute_b32 v18, v135, v4
	ds_bpermute_b32 v19, v135, v5
	v_accvgpr_read_b32 v9, a7
	v_accvgpr_read_b32 v8, a6
	v_accvgpr_read_b32 v7, a5
	v_accvgpr_read_b32 v6, a4
	s_and_saveexec_b64 s[52:53], vcc
	s_cbranch_execz .LBB1_232
	v_cmp_ne_u32_e32 vcc, 1, v136
	s_and_saveexec_b64 s[54:55], vcc
	s_xor_b64 s[54:55], exec, s[54:55]
	s_cbranch_execz .LBB1_229
	s_waitcnt lgkmcnt(0)
	v_cndmask_b32_e64 v16, v19, v18, s[2:3]

.LBB1_295:
	s_lshl_b32 s80, s79, 4
	v_or_b32_e32 v42, s80, v19
	s_andn2_b64 vcc, exec, s[52:53]
	v_lshlrev_b32_e32 v41, 2, v42
	s_cbranch_vccnz .LBB1_305
	v_or_b32_e32 v2, s80, v18
	v_mul_lo_u32 v44, v2, s78
	v_add3_u32 v4, v41, v44, s69
	v_mov_b32_e32 v8, v4
	s_nop 0
	ds_read2_b32 v[2:3], v8 offset1:68
	ds_read2_b32 v[4:5], v8 offset0:136 offset1:204
	v_accvgpr_write_b32 a4, v22
	v_accvgpr_write_b32 a5, v23
	v_accvgpr_write_b32 a6, v24
	s_waitcnt lgkmcnt(1)
	v_readlane_b32 s52, v2, 0
	v_accvgpr_write_b32 a7, v25
	v_cmp_lt_i32_e32 vcc, 0, v21
	v_rcp_f32_e64 v9, -s52
	v_cndmask_b32_e64 v8, 0, v2, s[4:5]
	v_mul_f32_e32 v6, v8, v9
	s_waitcnt lgkmcnt(0)
	s_nop 0
	v_mfma_f32_16x16x4_f32 v[2:5], v6, v2, v[2:5]
	v_mfma_f32_16x16x4_f32 a[4:7], v6, v22, a[4:7]
	s_nop 5
	v_readlane_b32 s52, v3, 1
	v_cndmask_b32_e64 v8, 0, v3, s[6:7]
	s_nop 0
	v_rcp_f32_e64 v9, -s52
	s_nop 0
	v_mul_f32_e32 v7, v8, v9
	s_nop 1
	v_mfma_f32_16x16x4_f32 v[2:5], v7, v3, v[2:5]
	v_mfma_f32_16x16x4_f32 a[4:7], v7, a5, a[4:7]
	s_nop 5
	v_readlane_b32 s52, v4, 2
	v_cndmask_b32_e64 v8, 0, v4, s[8:9]
	s_nop 0
	v_rcp_f32_e64 v9, -s52
	s_nop 0
	v_mul_f32_e32 v6, v8, v9
	s_nop 1
	v_mfma_f32_16x16x4_f32 v[2:5], v6, v4, v[2:5]
	v_mfma_f32_16x16x4_f32 a[4:7], v6, a6, a[4:7]
	s_nop 5
	v_readlane_b32 s52, v5, 3
	v_cndmask_b32_e64 v8, 0, v5, s[10:11]
	s_nop 0
	v_rcp_f32_e64 v9, -s52
	s_nop 0
	v_mul_f32_e32 v7, v8, v9
	s_nop 1
	v_mfma_f32_16x16x4_f32 v[2:5], v7, v5, v[2:5]
	v_mfma_f32_16x16x4_f32 a[4:7], v7, a7, a[4:7]
	s_nop 5
	v_readlane_b32 s52, v2, 20
	v_cndmask_b32_e64 v8, 0, v2, s[12:13]
	s_nop 0
	v_rcp_f32_e64 v9, -s52
	s_nop 0
	v_mul_f32_e32 v6, v8, v9
	s_nop 1
	v_mfma_f32_16x16x4_f32 v[2:5], v6, v2, v[2:5]
	v_mfma_f32_16x16x4_f32 a[4:7], v6, a4, a[4:7]
	s_nop 5
	v_readlane_b32 s52, v3, 21
	v_cndmask_b32_e64 v8, 0, v3, s[14:15]
	s_nop 0
	v_rcp_f32_e64 v9, -s52
	s_nop 0
	v_mul_f32_e32 v7, v8, v9
	s_nop 1
	v_mfma_f32_16x16x4_f32 v[2:5], v7, v3, v[2:5]
	v_mfma_f32_16x16x4_f32 a[4:7], v7, a5, a[4:7]
	s_nop 5
	v_readlane_b32 s52, v4, 22
	v_cndmask_b32_e64 v8, 0, v4, s[16:17]
	s_nop 0
	v_rcp_f32_e64 v9, -s52
	s_nop 0
	v_mul_f32_e32 v6, v8, v9
	s_nop 1
	v_mfma_f32_16x16x4_f32 v[2:5], v6, v4, v[2:5]
	v_mfma_f32_16x16x4_f32 a[4:7], v6, a6, a[4:7]
	s_nop 5
	v_readlane_b32 s52, v5, 23
	v_cndmask_b32_e64 v8, 0, v5, s[18:19]
	s_nop 0
	v_rcp_f32_e64 v9, -s52
	s_nop 0
	v_mul_f32_e32 v7, v8, v9
	s_nop 1
	v_mfma_f32_16x16x4_f32 v[2:5], v7, v5, v[2:5]
	v_mfma_f32_16x16x4_f32 a[4:7], v7, a7, a[4:7]
	s_nop 5
	v_readlane_b32 s52, v2, 40
	v_cndmask_b32_e64 v8, 0, v2, s[20:21]
	s_nop 0
	v_rcp_f32_e64 v9, -s52
	s_nop 0
	v_mul_f32_e32 v6, v8, v9
	s_nop 1
	v_mfma_f32_16x16x4_f32 v[2:5], v6, v2, v[2:5]
	v_mfma_f32_16x16x4_f32 a[4:7], v6, a4, a[4:7]
	s_nop 5
	v_readlane_b32 s52, v3, 41
	v_cndmask_b32_e64 v8, 0, v3, s[22:23]
	s_nop 0
	v_rcp_f32_e64 v9, -s52
	s_nop 0
	v_mul_f32_e32 v7, v8, v9
	s_nop 1
	v_mfma_f32_16x16x4_f32 v[2:5], v7, v3, v[2:5]
	v_mfma_f32_16x16x4_f32 a[4:7], v7, a5, a[4:7]
	s_nop 5
	v_readlane_b32 s52, v4, 42
	v_cndmask_b32_e64 v8, 0, v4, s[24:25]
	s_nop 0
	v_rcp_f32_e64 v9, -s52
	s_nop 0
	v_mul_f32_e32 v6, v8, v9
	s_nop 1
	v_mfma_f32_16x16x4_f32 v[2:5], v6, v4, v[2:5]
	v_mfma_f32_16x16x4_f32 a[4:7], v6, a6, a[4:7]
	s_nop 5
	v_readlane_b32 s52, v5, 43
	v_cndmask_b32_e64 v8, 0, v5, s[26:27]
	s_nop 0
	v_rcp_f32_e64 v9, -s52
	s_nop 0
	v_mul_f32_e32 v7, v8, v9
	s_nop 1
	v_mfma_f32_16x16x4_f32 v[2:5], v7, v5, v[2:5]
	v_mfma_f32_16x16x4_f32 a[4:7], v7, a7, a[4:7]
	s_nop 5
	v_readlane_b32 s52, v2, 60
	v_cndmask_b32_e64 v8, 0, v2, s[28:29]
	s_nop 0
	v_rcp_f32_e64 v9, -s52
	s_nop 0
	v_mul_f32_e32 v6, v8, v9
	s_nop 1
	v_mfma_f32_16x16x4_f32 v[2:5], v6, v2, v[2:5]
	v_mfma_f32_16x16x4_f32 a[4:7], v6, a4, a[4:7]
	s_nop 5
	v_readlane_b32 s52, v3, 61
	v_cndmask_b32_e64 v8, 0, v3, s[30:31]
	s_nop 0
	v_rcp_f32_e64 v9, -s52
	s_nop 0
	v_mul_f32_e32 v7, v8, v9
	s_nop 1
	v_mfma_f32_16x16x4_f32 v[2:5], v7, v3, v[2:5]
	v_mfma_f32_16x16x4_f32 a[4:7], v7, a5, a[4:7]
	s_nop 5
	v_readlane_b32 s52, v4, 62
	v_cndmask_b32_e64 v8, 0, v4, s[34:35]
	s_nop 0
	v_rcp_f32_e64 v9, -s52
	s_nop 0
	v_mul_f32_e32 v6, v8, v9
	s_nop 1
	v_mfma_f32_16x16x4_f32 v[2:5], v6, v4, v[2:5]
	v_mfma_f32_16x16x4_f32 a[4:7], v6, a6, a[4:7]
	s_nop 5
	ds_bpermute_b32 v53, v20, v2
	ds_bpermute_b32 v54, v20, v3
	ds_bpermute_b32 v55, v20, v4
	ds_bpermute_b32 v56, v20, v5
	v_accvgpr_read_b32 v9, a7
	v_accvgpr_read_b32 v8, a6
	v_accvgpr_read_b32 v7, a5
	v_accvgpr_read_b32 v6, a4
	s_and_saveexec_b64 s[52:53], vcc
	s_cbranch_execz .LBB1_302
	v_cmp_ne_u32_e32 vcc, 1, v21
	s_and_saveexec_b64 s[58:59], vcc
	s_xor_b64 s[58:59], exec, s[58:59]
	s_cbranch_execz .LBB1_299
	s_waitcnt lgkmcnt(0)
	v_cndmask_b32_e64 v53, v56, v55, s[0:1]

.LBB1_336:
	s_lshl_b32 s75, s74, 4
	v_or_b32_e32 v34, s75, v19
	s_andn2_b64 vcc, exec, s[52:53]
	v_lshlrev_b32_e32 v14, 2, v34
	s_cbranch_vccnz .LBB1_346
	v_or_b32_e32 v0, s75, v18
	v_mul_lo_u32 v35, v0, s64
	v_add3_u32 v2, v14, v35, s72
	v_mov_b32_e32 v6, v2
	s_nop 0
	ds_read2_b32 v[0:1], v6 offset1:68
	ds_read2_b32 v[2:3], v6 offset0:136 offset1:204
	v_accvgpr_write_b32 a4, v22
	v_accvgpr_write_b32 a5, v23
	v_accvgpr_write_b32 a6, v24
	s_waitcnt lgkmcnt(1)
	v_readlane_b32 s52, v0, 0
	v_accvgpr_write_b32 a7, v25
	v_cmp_lt_i32_e32 vcc, 0, v21
	v_rcp_f32_e64 v7, -s52
	v_cndmask_b32_e64 v6, 0, v0, s[4:5]
	v_mul_f32_e32 v4, v6, v7
	s_waitcnt lgkmcnt(0)
	s_nop 0
	v_mfma_f32_16x16x4_f32 v[0:3], v4, v0, v[0:3]
	v_mfma_f32_16x16x4_f32 a[4:7], v4, v22, a[4:7]
	s_nop 5
	v_readlane_b32 s52, v1, 1
	v_cndmask_b32_e64 v6, 0, v1, s[6:7]
	s_nop 0
	v_rcp_f32_e64 v7, -s52
	s_nop 0
	v_mul_f32_e32 v5, v6, v7
	s_nop 1
	v_mfma_f32_16x16x4_f32 v[0:3], v5, v1, v[0:3]
	v_mfma_f32_16x16x4_f32 a[4:7], v5, a5, a[4:7]
	s_nop 5
	v_readlane_b32 s52, v2, 2
	v_cndmask_b32_e64 v6, 0, v2, s[8:9]
	s_nop 0
	v_rcp_f32_e64 v7, -s52
	s_nop 0
	v_mul_f32_e32 v4, v6, v7
	s_nop 1
	v_mfma_f32_16x16x4_f32 v[0:3], v4, v2, v[0:3]
	v_mfma_f32_16x16x4_f32 a[4:7], v4, a6, a[4:7]
	s_nop 5
	v_readlane_b32 s52, v3, 3
	v_cndmask_b32_e64 v6, 0, v3, s[10:11]
	s_nop 0
	v_rcp_f32_e64 v7, -s52
	s_nop 0
	v_mul_f32_e32 v5, v6, v7
	s_nop 1
	v_mfma_f32_16x16x4_f32 v[0:3], v5, v3, v[0:3]
	v_mfma_f32_16x16x4_f32 a[4:7], v5, a7, a[4:7]
	s_nop 5
	v_readlane_b32 s52, v0, 20
	v_cndmask_b32_e64 v6, 0, v0, s[12:13]
	s_nop 0
	v_rcp_f32_e64 v7, -s52
	s_nop 0
	v_mul_f32_e32 v4, v6, v7
	s_nop 1
	v_mfma_f32_16x16x4_f32 v[0:3], v4, v0, v[0:3]
	v_mfma_f32_16x16x4_f32 a[4:7], v4, a4, a[4:7]
	s_nop 5
	v_readlane_b32 s52, v1, 21
	v_cndmask_b32_e64 v6, 0, v1, s[14:15]
	s_nop 0
	v_rcp_f32_e64 v7, -s52
	s_nop 0
	v_mul_f32_e32 v5, v6, v7
	s_nop 1
	v_mfma_f32_16x16x4_f32 v[0:3], v5, v1, v[0:3]
	v_mfma_f32_16x16x4_f32 a[4:7], v5, a5, a[4:7]
	s_nop 5
	v_readlane_b32 s52, v2, 22
	v_cndmask_b32_e64 v6, 0, v2, s[16:17]
	s_nop 0
	v_rcp_f32_e64 v7, -s52
	s_nop 0
	v_mul_f32_e32 v4, v6, v7
	s_nop 1
	v_mfma_f32_16x16x4_f32 v[0:3], v4, v2, v[0:3]
	v_mfma_f32_16x16x4_f32 a[4:7], v4, a6, a[4:7]
	s_nop 5
	v_readlane_b32 s52, v3, 23
	v_cndmask_b32_e64 v6, 0, v3, s[18:19]
	s_nop 0
	v_rcp_f32_e64 v7, -s52
	s_nop 0
	v_mul_f32_e32 v5, v6, v7
	s_nop 1
	v_mfma_f32_16x16x4_f32 v[0:3], v5, v3, v[0:3]
	v_mfma_f32_16x16x4_f32 a[4:7], v5, a7, a[4:7]
	s_nop 5
	v_readlane_b32 s52, v0, 40
	v_cndmask_b32_e64 v6, 0, v0, s[20:21]
	s_nop 0
	v_rcp_f32_e64 v7, -s52
	s_nop 0
	v_mul_f32_e32 v4, v6, v7
	s_nop 1
	v_mfma_f32_16x16x4_f32 v[0:3], v4, v0, v[0:3]
	v_mfma_f32_16x16x4_f32 a[4:7], v4, a4, a[4:7]
	s_nop 5
	v_readlane_b32 s52, v1, 41
	v_cndmask_b32_e64 v6, 0, v1, s[22:23]
	s_nop 0
	v_rcp_f32_e64 v7, -s52
	s_nop 0
	v_mul_f32_e32 v5, v6, v7
	s_nop 1
	v_mfma_f32_16x16x4_f32 v[0:3], v5, v1, v[0:3]
	v_mfma_f32_16x16x4_f32 a[4:7], v5, a5, a[4:7]
	s_nop 5
	v_readlane_b32 s52, v2, 42
	v_cndmask_b32_e64 v6, 0, v2, s[24:25]
	s_nop 0
	v_rcp_f32_e64 v7, -s52
	s_nop 0
	v_mul_f32_e32 v4, v6, v7
	s_nop 1
	v_mfma_f32_16x16x4_f32 v[0:3], v4, v2, v[0:3]
	v_mfma_f32_16x16x4_f32 a[4:7], v4, a6, a[4:7]
	s_nop 5
	v_readlane_b32 s52, v3, 43
	v_cndmask_b32_e64 v6, 0, v3, s[26:27]
	s_nop 0
	v_rcp_f32_e64 v7, -s52
	s_nop 0
	v_mul_f32_e32 v5, v6, v7
	s_nop 1
	v_mfma_f32_16x16x4_f32 v[0:3], v5, v3, v[0:3]
	v_mfma_f32_16x16x4_f32 a[4:7], v5, a7, a[4:7]
	s_nop 5
	v_readlane_b32 s52, v0, 60
	v_cndmask_b32_e64 v6, 0, v0, s[28:29]
	s_nop 0
	v_rcp_f32_e64 v7, -s52
	s_nop 0
	v_mul_f32_e32 v4, v6, v7
	s_nop 1
	v_mfma_f32_16x16x4_f32 v[0:3], v4, v0, v[0:3]
	v_mfma_f32_16x16x4_f32 a[4:7], v4, a4, a[4:7]
	s_nop 5
	v_readlane_b32 s52, v1, 61
	v_cndmask_b32_e64 v6, 0, v1, s[30:31]
	s_nop 0
	v_rcp_f32_e64 v7, -s52
	s_nop 0
	v_mul_f32_e32 v5, v6, v7
	s_nop 1
	v_mfma_f32_16x16x4_f32 v[0:3], v5, v1, v[0:3]
	v_mfma_f32_16x16x4_f32 a[4:7], v5, a5, a[4:7]
	s_nop 5
	v_readlane_b32 s52, v2, 62
	v_cndmask_b32_e64 v6, 0, v2, s[34:35]
	s_nop 0
	v_rcp_f32_e64 v7, -s52
	s_nop 0
	v_mul_f32_e32 v4, v6, v7
	s_nop 1
	v_mfma_f32_16x16x4_f32 v[0:3], v4, v2, v[0:3]
	v_mfma_f32_16x16x4_f32 a[4:7], v4, a6, a[4:7]
	s_nop 5
	ds_bpermute_b32 v36, v20, v0
	ds_bpermute_b32 v37, v20, v1
	ds_bpermute_b32 v43, v20, v2
	ds_bpermute_b32 v45, v20, v3
	v_accvgpr_read_b32 v7, a7
	v_accvgpr_read_b32 v6, a6
	v_accvgpr_read_b32 v5, a5
	v_accvgpr_read_b32 v4, a4
	s_and_saveexec_b64 s[52:53], vcc
	s_cbranch_execz .LBB1_343
	v_cmp_ne_u32_e32 vcc, 1, v21
	s_and_saveexec_b64 s[54:55], vcc
	s_xor_b64 s[54:55], exec, s[54:55]
	s_cbranch_execz .LBB1_340
	s_waitcnt lgkmcnt(0)
	v_cndmask_b32_e64 v36, v45, v43, s[0:1]
